# re-deal context qkv tiles and surplus pool GEMM units to the workgroups with two scan units
# speedup vs baseline: 1.0054x; 1.0054x over previous
.LBB0_986:
	s_waitcnt lgkmcnt(0)
	s_load_dwordx4 s[0:3], s[74:75], 0xa8
	v_and_b32_e32 v18, 31, v0
	v_lshlrev_b32_e32 v46, 3, v18
	v_cmp_gt_u32_e64 s[6:7], 24, v18
	s_ashr_i32 s33, s90, 31
	v_lshlrev_b32_e32 v69, 4, v0
	v_cndmask_b32_e64 v2, 0, v46, s[6:7]
	v_lshlrev_b32_e32 v19, 2, v2
	s_waitcnt lgkmcnt(0)
	global_load_dwordx4 v[2:5], v19, s[0:1] offset:16
	global_load_dwordx4 v[6:9], v19, s[2:3] offset:16
	global_load_dwordx4 v[10:13], v19, s[0:1]
	global_load_dwordx4 v[14:17], v19, s[2:3]
	s_abs_i32 s0, s90
	v_cvt_f32_u32_e32 v19, s0
	s_sub_i32 s3, 0, s0
	s_add_i32 s1, s90, 0x1ff
	s_ashr_i32 s2, s1, 31
	v_rcp_iflag_f32_e32 v19, v19
	s_abs_i32 s1, s1
	s_xor_b32 s2, s2, s33
	v_mul_f32_e32 v19, 0x4f7ffffe, v19
	v_cvt_u32_f32_e32 v19, v19
	s_barrier
	v_readfirstlane_b32 s4, v19
	s_mul_i32 s3, s3, s4
	s_mul_hi_u32 s3, s4, s3
	s_add_i32 s4, s4, s3
	s_mul_hi_u32 s3, s1, s4
	s_mul_i32 s5, s3, s0
	s_sub_i32 s1, s1, s5
	s_add_i32 s5, s3, 1
	s_sub_i32 s8, s1, s0
	s_cmp_ge_u32 s1, s0
	s_cselect_b32 s3, s5, s3
	s_cselect_b32 s1, s8, s1
	s_add_i32 s5, s3, 1
	s_cmp_ge_u32 s1, s0
	s_cselect_b32 s1, s5, s3
	s_xor_b32 s1, s1, s2
	s_sub_i32 s3, s1, s2
	s_add_i32 s1, s90, 63
	s_ashr_i32 s2, s1, 31
	s_abs_i32 s1, s1
	s_mul_hi_u32 s4, s1, s4
	s_mul_i32 s5, s4, s0
	s_sub_i32 s1, s1, s5
	s_xor_b32 s2, s2, s33
	s_add_i32 s5, s4, 1
	s_sub_i32 s8, s1, s0
	s_cmp_ge_u32 s1, s0
	s_cselect_b32 s4, s5, s4
	s_cselect_b32 s1, s8, s1
	s_add_i32 s5, s4, 1
	s_cmp_ge_u32 s1, s0
	s_cselect_b32 s0, s5, s4
	s_xor_b32 s0, s0, s2
	s_sub_i32 s28, s0, s2
	s_add_i32 s28, s28, s3
	s_cmp_gt_i32 s28, 0
	s_cbranch_scc1 .LBB0_988
	s_not_b32 s0, s88
	s_mov_b32 s36, s88
	v_lshrrev_b32_e32 v96, 2, v0
	v_and_b32_e32 v48, 48, v69
	s_cbranch_execz .LBB0_989
	s_branch .LBB0_1043

.LBB0_989:
	v_and_b32_e32 v19, 24, v0
	v_cmp_eq_u32_e64 s[8:9], 16, v19
	v_cmp_ne_u32_e64 s[10:11], 16, v19
	v_and_b32_e32 v19, 2, v0
	v_cmp_eq_u32_e64 s[12:13], 0, v19
	v_lshrrev_b32_e32 v19, 5, v162
	v_add_u32_e32 v22, -16, v18
	v_lshlrev_b32_e32 v20, 3, v22
	v_cmp_gt_u32_e64 s[14:15], 4, v22
	v_mul_u32_u24_e32 v22, 0xc0, v19
	v_mul_u32_u24_e32 v26, 0x140, v19
	v_or_b32_e32 v19, 64, v162
	v_lshrrev_b32_e32 v19, 4, v19
	v_mul_u32_u24_e32 v29, 0x140, v19
	v_xor_b32_e32 v19, v69, v0
	v_lshrrev_b32_e32 v24, 3, v19
	v_lshlrev_b32_e32 v19, 1, v19
	v_mov_b32_e32 v47, 0
	v_and_b32_e32 v19, 32, v19
	v_and_or_b32 v19, v24, 4, v19
	v_lshlrev_b32_e32 v24, 6, v96
	v_mov_b32_e32 v25, v47
	v_lshl_add_u64 v[24:25], s[86:87], 0, v[24:25]
	v_mov_b32_e32 v49, v47
	v_mul_u32_u24_e32 v19, 0x300, v19
	v_lshl_add_u64 v[24:25], v[24:25], 0, v[48:49]
	s_mov_b64 s[4:5], 0x6c800000
	v_add3_u32 v98, 0, v96, v19
	v_lshl_add_u64 v[50:51], v[24:25], 0, s[4:5]
	v_lshlrev_b32_e32 v18, 4, v18
	v_mov_b32_e32 v19, v47
	v_lshlrev_b32_e32 v24, 1, v26
	v_mov_b32_e32 v25, v47
	v_lshl_add_u64 v[26:27], v[18:19], 0, v[24:25]
	s_mov_b64 s[4:5], 0x4ac00500
	v_mov_b32_e32 v21, v47
	v_lshl_add_u64 v[52:53], v[26:27], 0, s[4:5]
	v_mov_b64_e32 v[26:27], 0x34401c00
	v_mul_u32_u24_e32 v28, 0x140, v1
	v_lshl_add_u64 v[54:55], v[20:21], 1, v[26:27]
	v_lshl_add_u64 v[20:21], v[46:47], 0, v[24:25]
	v_lshl_add_u64 v[56:57], v[20:21], 0, s[4:5]
	v_lshlrev_b32_e32 v20, 4, v189
	v_mov_b32_e32 v21, v47
	v_lshlrev_b32_e32 v24, 1, v28
	v_lshl_add_u64 v[24:25], v[20:21], 0, v[24:25]
	s_mov_b64 s[4:5], 0x4ac00180
	v_lshl_add_u64 v[60:61], v[24:25], 0, s[4:5]
	v_lshlrev_b32_e32 v24, 1, v29
	v_mov_b32_e32 v25, v47
	v_lshl_add_u64 v[20:21], v[20:21], 0, v[24:25]
	v_lshl_add_u64 v[62:63], v[20:21], 0, s[4:5]
	v_lshlrev_b32_e32 v20, 1, v22
	v_mov_b32_e32 v21, v47
	s_add_u32 s0, s86, 0x298000
	v_mov_b32_e32 v23, v47
	v_lshl_add_u64 v[18:19], v[18:19], 0, v[20:21]
	s_mov_b64 s[4:5], 0x45200300
	s_addc_u32 s1, s87, 0
	s_not_b32 s2, s88
	v_lshl_add_u64 v[64:65], v[18:19], 0, s[4:5]
	v_lshl_add_u64 v[18:19], v[46:47], 0, v[22:23]
	s_mov_b64 s[4:5], 0x45200180
	s_mov_b32 s36, s88
	s_bfe_u32 s2, s92, 0x30006
	v_lshl_add_u64 v[66:67], v[18:19], 0, s[4:5]
	v_mbcnt_lo_u32_b32 v18, -1, 0
	s_lshl_b32 s31, s2, 3
	s_mulk_i32 s2, 0x1800
	v_mbcnt_hi_u32_b32 v99, -1, v18
	s_add_i32 s2, s2, 0
	v_and_b32_e32 v18, 64, v99
	v_and_b32_e32 v97, 16, v69
	s_mov_b32 s29, 0
	v_cmp_gt_u32_e64 s[16:17], 32, v162
	s_lshl_b32 s30, s83, 3
	v_lshl_add_u32 v49, v162, 3, s2
	v_lshlrev_b32_e32 v58, 4, v162
	v_mov_b32_e32 v59, v47
	s_mov_b32 s2, 0x3b000000
	s_mov_b32 s34, 0x800000
	s_mov_b32 s35, 0xc3e00000
	v_mov_b32_e32 v68, 0x358637bd
	s_mov_b64 s[4:5], 0x1000
	s_mov_b64 s[20:21], 0x1e00
	s_mov_b64 s[22:23], 0xa00
	v_add_u32_e32 v100, 64, v18
	v_xor_b32_e32 v101, 1, v99
	v_xor_b32_e32 v102, 2, v99
	v_xor_b32_e32 v103, 4, v99
	v_xor_b32_e32 v104, 8, v99
	v_xor_b32_e32 v105, 16, v99
	v_xor_b32_e32 v106, 32, v99
	v_mov_b32_e32 v107, 0x1e00
	v_mov_b32_e32 v108, 0xa00
	v_mov_b32_e32 v109, 0x43e00000
	s_branch .LBB0_992

.LBB0_1458:
	s_add_u32 s14, s86, 0x34400000
	s_addc_u32 s15, s87, 0
	s_add_u32 s4, s86, 0x900000
	s_addc_u32 s5, s87, 0
	s_add_u32 s8, s86, 0x940000
	s_addc_u32 s9, s87, 0
	s_lshl_b32 s10, s10, 5
	s_and_b32 s18, s10, 0x60
	s_mov_b64 s[10:11], 0x80
	s_add_i32 m0, s39, 0x18000
	v_lshl_add_u64 v[8:9], v[8:9], 0, s[10:11]
	s_lshl_b32 s13, s12, 13
	s_lshl_b32 s19, s18, 7
	s_ashr_i32 s44, s88, 31
	s_waitcnt vmcnt(2)
	s_barrier
	global_load_lds_dwordx4 v[8:9], off
	v_lshl_add_u64 v[6:7], v[6:7], 0, s[10:11]
	s_add_i32 m0, s39, 0x1a000
	s_add_i32 s45, s39, 0x8000
	s_add_i32 s46, s39, 0xa000
	global_load_lds_dwordx4 v[6:7], off
	v_lshl_add_u64 v[2:3], v[2:3], 0, s[10:11]
	s_mov_b32 m0, s45
	s_add_u32 s16, s28, 0x40080
	global_load_lds_dwordx4 v[2:3], off
	v_lshl_add_u64 v[2:3], v[4:5], 0, s[10:11]
	s_mov_b32 m0, s46
	s_addc_u32 s17, s29, 0
	global_load_lds_dwordx4 v[2:3], off
	s_add_i32 m0, s39, 0x1c000
	v_lshl_add_u64 v[2:3], s[16:17], 0, v[148:149]
	global_load_lds_dwordx4 v[2:3], off
	v_lshl_add_u64 v[2:3], s[16:17], 0, v[152:153]
	s_add_i32 m0, s39, 0x1e000
	s_sext_i32_i16 s25, s6
	global_load_lds_dwordx4 v[2:3], off
	v_and_b32_e32 v2, 15, v0
	v_lshlrev_b32_e32 v3, 1, v14
	v_lshlrev_b32_e32 v4, 6, v0
	s_movk_i32 s6, 0x3c0
	v_lshlrev_b32_e32 v5, 2, v0
	v_and_or_b32 v4, v4, s6, v3
	v_and_b32_e32 v5, 32, v5
	v_lshl_or_b32 v154, s12, 6, v2
	v_lshl_or_b32 v2, v2, 6, v3
	v_mov_b32_e32 v155, v149
	v_bitop3_b32 v22, v2, s13, v5 bitop3:0xde
	v_bitop3_b32 v185, s19, v4, v5 bitop3:0xf6
	v_lshlrev_b64 v[2:3], 7, v[154:155]
	v_or_b32_e32 v4, 16, v154
	v_mov_b32_e32 v5, v149
	v_or_b32_e32 v156, s18, v14
	v_mov_b32_e32 v157, v149
	v_lshlrev_b64 v[4:5], 7, v[4:5]
	v_or_b32_e32 v6, 32, v154
	v_mov_b32_e32 v7, v149
	v_lshl_add_u64 v[2:3], s[14:15], 0, v[2:3]
	v_lshlrev_b64 v[6:7], 7, v[6:7]
	v_or_b32_e32 v8, 48, v154
	v_mov_b32_e32 v9, v149
	v_lshl_add_u64 v[158:159], v[2:3], 0, v[156:157]
	v_lshl_add_u64 v[2:3], s[14:15], 0, v[4:5]
	v_lshlrev_b64 v[8:9], 7, v[8:9]
	v_add_u32_e32 v14, 0x80, v154
	v_mov_b32_e32 v15, v149
	v_lshl_add_u64 v[160:161], v[2:3], 0, v[156:157]
	v_lshl_add_u64 v[2:3], s[14:15], 0, v[6:7]
	v_lshlrev_b64 v[14:15], 7, v[14:15]
	v_add_u32_e32 v16, 0x90, v154
	v_mov_b32_e32 v17, v149
	v_lshl_add_u64 v[164:165], v[2:3], 0, v[156:157]
	v_lshl_add_u64 v[2:3], s[14:15], 0, v[8:9]
	v_lshlrev_b64 v[16:17], 7, v[16:17]
	v_add_u32_e32 v18, 0xa0, v154
	v_mov_b32_e32 v19, v149
	v_lshl_add_u64 v[166:167], v[2:3], 0, v[156:157]
	v_lshl_add_u64 v[2:3], s[14:15], 0, v[14:15]
	v_lshlrev_b64 v[18:19], 7, v[18:19]
	v_add_u32_e32 v20, 0xb0, v154
	v_mov_b32_e32 v21, v149
	v_lshl_add_u64 v[168:169], v[2:3], 0, v[156:157]
	v_lshl_add_u64 v[2:3], s[14:15], 0, v[16:17]
	v_lshlrev_b64 v[20:21], 7, v[20:21]
	v_lshl_add_u64 v[170:171], v[2:3], 0, v[156:157]
	v_lshl_add_u64 v[2:3], s[14:15], 0, v[18:19]
	v_lshl_add_u64 v[172:173], v[2:3], 0, v[156:157]
	v_lshl_add_u64 v[2:3], s[14:15], 0, v[20:21]
	v_lshl_add_u64 v[174:175], v[2:3], 0, v[156:157]
	v_lshlrev_b32_e32 v2, 8, v0
	v_and_b32_e32 v2, 0x18000, v2
	v_lshlrev_b32_e32 v3, 11, v12
	v_or3_b32 v2, v10, v2, v3
	v_add_u32_e32 v176, v2, v11
	v_lshlrev_b32_e32 v2, 4, v13
	s_waitcnt vmcnt(6)
	s_cmpk_lt_u32 s7, 0x100
	v_and_b32_e32 v2, 0x38000, v2
	s_cselect_b64 s[12:13], -1, 0
	v_or3_b32 v2, v10, v2, v3
	s_add_i32 s15, 0, 0x10000
	s_add_i32 s48, 0, 0x14000
	s_ashr_i32 s47, s90, 31
	v_mov_b32_e32 v177, v149
	v_add_u32_e32 v178, v2, v11
	v_mov_b32_e32 v179, v149
	v_mov_b64_e32 v[180:181], 0x18c0
	v_mov_b64_e32 v[182:183], 0x18bf
	v_add_u32_e32 v155, s15, v185
	v_add_u32_e32 v157, s48, v185
	v_add_u32_e32 v186, 0, v22
	s_mov_b32 s14, 0xbfb8aa3b
	s_mov_b32 s49, 0xc3e00000
	v_mov_b32_e32 v187, 0x43e00000
	s_barrier
	s_branch .LBB0_1461

.LBB0_1461:
	s_add_i32 s43, s43, 1
	s_mul_i32 s6, s43, s47
	s_mul_hi_u32 s7, s43, s90
	s_add_i32 s7, s7, s6
	s_mul_i32 s6, s43, s90
	s_add_u32 s20, s6, s88
	s_addc_u32 s21, s7, s44
	v_cmp_gt_i64_e32 vcc, s[20:21], v[182:183]
	v_cmp_lt_i64_e64 s[6:7], s[20:21], v[180:181]
	s_cbranch_vccnz .LBB0_1463
	s_mul_i32 s19, s21, 0x95fad40b
	s_mul_hi_u32 s22, s20, 0x95fad40b
	s_mul_hi_u32 s18, s21, 0x95fad40b
	s_add_u32 s19, s19, s22
	s_mul_i32 s17, s20, 0xa57eb502
	s_addc_u32 s18, s18, 0
	s_mul_hi_u32 s16, s20, 0xa57eb502
	s_add_u32 s17, s17, s19
	s_addc_u32 s16, s16, 0
	s_add_u32 s16, s18, s16
	s_addc_u32 s17, 0, 0
	s_mul_i32 s19, s21, 0xa57eb502
	s_mul_hi_u32 s18, s21, 0xa57eb502
	s_add_u32 s16, s19, s16
	s_addc_u32 s17, s18, s17
	s_ashr_i32 s18, s21, 31
	s_mul_i32 s19, s18, 0xa57eb502
	s_mul_hi_u32 s22, s18, 0x95fad40b
	s_add_i32 s19, s22, s19
	s_mul_i32 s18, s18, 0x95fad40b
	s_add_i32 s19, s19, s18
	s_sub_u32 s18, s18, s20
	s_subb_u32 s19, s19, s21
	s_add_u32 s16, s16, s18
	s_addc_u32 s17, s17, s19
	s_add_u32 s16, s16, s20
	s_addc_u32 s17, s17, s21
	s_ashr_i64 s[18:19], s[16:17], 12
	s_lshr_b32 s16, s17, 31
	s_add_u32 s16, s18, s16
	s_mulk_i32 s16, 0x18c0
	s_sub_i32 s16, s20, s16
	s_sext_i32_i16 s17, s16
	s_bfe_u32 s17, s17, 0x3001c
	s_add_i32 s17, s16, s17
	s_sext_i32_i16 s18, s17
	s_and_b32 s17, s17, 0xfff8
	s_sub_i32 s16, s16, s17
	s_ashr_i32 s18, s18, 3
	s_sext_i32_i16 s17, s16
	s_cmp_lt_i32 s17, 0
	s_cselect_b32 s17, s38, 0x318
	s_mul_i32 s16, s17, s16
	s_add_i32 s16, s16, s18
	s_sext_i32_i16 s17, s16
	s_mulk_i32 s17, 0xba3
	s_lshr_b32 s18, s17, 31
	s_ashr_i32 s17, s17, 19
	s_add_i32 s17, s17, s18
	s_lshl_b32 s18, s17, 2
	s_mulk_i32 s17, 0xb0
	s_sub_i32 s16, s16, s17
	s_sext_i32_i16 s17, s16
	s_bfe_u32 s17, s17, 0x2001d
	s_add_i32 s17, s16, s17
	s_sext_i32_i16 s19, s17
	s_and_b32 s17, s17, 0xfffc
	s_sub_i32 s16, s16, s17
	s_sext_i32_i16 s16, s16
	s_add_i32 s16, s18, s16
	s_ashr_i32 s18, s19, 2

.LBB0_1464:
	ds_read_b128 v[94:97], v155
	ds_read_b128 v[98:101], v155 offset:1024
	ds_read_b128 v[106:109], v155 offset:2048
	ds_read_b128 v[110:113], v155 offset:3072
	ds_read_b128 v[188:191], v157
	ds_read_b128 v[192:195], v157 offset:1024
	ds_read_b128 v[196:199], v157 offset:2048
	ds_read_b128 v[200:203], v157 offset:3072
	s_add_u32 s28, s26, 0xfffc0080
	s_addc_u32 s29, s27, -1
	s_cmp_eq_u32 s54, 12
	s_cselect_b32 s31, s17, s29
	s_cselect_b32 s30, s50, s28
	s_cselect_b32 s29, s19, s53
	s_cselect_b32 s28, s51, s52
	v_lshl_add_u64 v[236:237], s[26:27], 0, v[176:177]
	s_add_i32 m0, s39, 0xc000
	ds_read_b128 v[204:207], v186
	ds_read_b128 v[208:211], v186 offset:1024
	ds_read_b128 v[212:215], v186 offset:2048
	ds_read_b128 v[216:219], v186 offset:3072
	ds_read_b128 v[220:223], v186 offset:4096
	ds_read_b128 v[224:227], v186 offset:5120
	ds_read_b128 v[228:231], v186 offset:6144
	ds_read_b128 v[232:235], v186 offset:7168
	global_load_lds_dwordx4 v[236:237], off
	v_lshl_add_u64 v[236:237], s[26:27], 0, v[178:179]
	s_add_i32 m0, s39, 0xe000
	s_nop 0
	global_load_lds_dwordx4 v[236:237], off
	s_waitcnt vmcnt(8)
	s_waitcnt lgkmcnt(0)
	s_barrier
	s_setprio 1
	s_waitcnt lgkmcnt(0)
	v_mfma_i32_16x16x64_i8 v[142:145], v[94:97], v[204:207], v[142:145]
	v_mfma_i32_16x16x64_i8 v[134:137], v[106:109], v[204:207], v[134:137]
	v_mfma_i32_16x16x64_i8 v[126:129], v[94:97], v[212:215], v[126:129]
	v_mfma_i32_16x16x64_i8 v[118:121], v[106:109], v[212:215], v[118:121]
	v_mfma_i32_16x16x64_i8 v[102:105], v[94:97], v[220:223], v[102:105]
	v_mfma_i32_16x16x64_i8 v[86:89], v[106:109], v[220:223], v[86:89]
	v_mfma_i32_16x16x64_i8 v[78:81], v[94:97], v[228:231], v[78:81]
	v_mfma_i32_16x16x64_i8 v[70:73], v[106:109], v[228:231], v[70:73]
	v_mfma_i32_16x16x64_i8 v[142:145], v[98:101], v[208:211], v[142:145]
	v_mfma_i32_16x16x64_i8 v[134:137], v[110:113], v[208:211], v[134:137]
	v_mfma_i32_16x16x64_i8 v[126:129], v[98:101], v[216:219], v[126:129]
	v_mfma_i32_16x16x64_i8 v[118:121], v[110:113], v[216:219], v[118:121]
	v_mfma_i32_16x16x64_i8 v[102:105], v[98:101], v[224:227], v[102:105]
	v_mfma_i32_16x16x64_i8 v[86:89], v[110:113], v[224:227], v[86:89]
	v_mfma_i32_16x16x64_i8 v[78:81], v[98:101], v[232:235], v[78:81]
	v_mfma_i32_16x16x64_i8 v[70:73], v[110:113], v[232:235], v[70:73]
	s_setprio 0
	s_setprio 1
	v_mfma_i32_16x16x64_i8 v[138:141], v[188:191], v[204:207], v[138:141]
	v_mfma_i32_16x16x64_i8 v[130:133], v[196:199], v[204:207], v[130:133]
	v_mfma_i32_16x16x64_i8 v[122:125], v[188:191], v[212:215], v[122:125]
	v_mfma_i32_16x16x64_i8 v[114:117], v[196:199], v[212:215], v[114:117]
	v_mfma_i32_16x16x64_i8 v[90:93], v[188:191], v[220:223], v[90:93]
	v_mfma_i32_16x16x64_i8 v[82:85], v[196:199], v[220:223], v[82:85]
	v_mfma_i32_16x16x64_i8 v[74:77], v[188:191], v[228:231], v[74:77]
	v_mfma_i32_16x16x64_i8 v[66:69], v[196:199], v[228:231], v[66:69]
	v_mfma_i32_16x16x64_i8 v[138:141], v[192:195], v[208:211], v[138:141]
	v_mfma_i32_16x16x64_i8 v[130:133], v[200:203], v[208:211], v[130:133]
	v_mfma_i32_16x16x64_i8 v[122:125], v[192:195], v[216:219], v[122:125]
	v_mfma_i32_16x16x64_i8 v[114:117], v[200:203], v[216:219], v[114:117]
	v_mfma_i32_16x16x64_i8 v[90:93], v[192:195], v[224:227], v[90:93]
	v_mfma_i32_16x16x64_i8 v[82:85], v[200:203], v[224:227], v[82:85]
	v_mfma_i32_16x16x64_i8 v[74:77], v[192:195], v[232:235], v[74:77]
	v_mfma_i32_16x16x64_i8 v[66:69], v[200:203], v[232:235], v[66:69]
	s_setprio 0
	s_barrier
	s_add_i32 s55, s15, s37
	v_lshl_add_u64 v[236:237], s[28:29], 0, v[148:149]
	s_mov_b32 m0, s55
	ds_read_b128 v[204:207], v186 offset:16384
	ds_read_b128 v[208:211], v186 offset:17408
	ds_read_b128 v[212:215], v186 offset:18432
	ds_read_b128 v[216:219], v186 offset:19456
	ds_read_b128 v[220:223], v186 offset:20480
	ds_read_b128 v[224:227], v186 offset:21504
	ds_read_b128 v[228:231], v186 offset:22528
	ds_read_b128 v[232:235], v186 offset:23552
	global_load_lds_dwordx4 v[236:237], off
	s_add_i32 m0, s55, 0x2000
	s_add_u32 s56, s28, 0x40000
	v_lshl_add_u64 v[238:239], s[28:29], 0, v[152:153]
	s_addc_u32 s57, s29, 0
	s_add_i32 s55, s48, s37
	global_load_lds_dwordx4 v[238:239], off
	v_lshl_add_u64 v[240:241], s[56:57], 0, v[148:149]
	s_mov_b32 m0, s55
	v_lshl_add_u64 v[242:243], s[30:31], 0, v[150:151]
	global_load_lds_dwordx4 v[240:241], off
	v_lshl_add_u64 v[240:241], s[56:57], 0, v[152:153]
	s_add_i32 m0, s55, 0x2000
	s_nop 0
	global_load_lds_dwordx4 v[240:241], off
	v_lshl_add_u64 v[240:241], s[30:31], 0, v[146:147]
	s_mov_b32 m0, s39
	s_nop 0
	global_load_lds_dwordx4 v[240:241], off
	s_mov_b32 m0, s40
	s_nop 0
	global_load_lds_dwordx4 v[242:243], off
	s_waitcnt vmcnt(8)
	s_waitcnt lgkmcnt(0)
	s_barrier
	s_setprio 1
	s_waitcnt lgkmcnt(0)
	v_mfma_i32_16x16x64_i8 v[62:65], v[94:97], v[204:207], v[62:65]
	v_mfma_i32_16x16x64_i8 v[54:57], v[106:109], v[204:207], v[54:57]
	v_mfma_i32_16x16x64_i8 v[46:49], v[94:97], v[212:215], v[46:49]
	v_mfma_i32_16x16x64_i8 v[38:41], v[106:109], v[212:215], v[38:41]
	v_mfma_i32_16x16x64_i8 v[30:33], v[94:97], v[220:223], v[30:33]
	v_mfma_i32_16x16x64_i8 v[22:25], v[106:109], v[220:223], v[22:25]
	v_mfma_i32_16x16x64_i8 v[14:17], v[94:97], v[228:231], v[14:17]
	v_mfma_i32_16x16x64_i8 v[6:9], v[106:109], v[228:231], v[6:9]
	v_mfma_i32_16x16x64_i8 v[62:65], v[98:101], v[208:211], v[62:65]
	v_mfma_i32_16x16x64_i8 v[54:57], v[110:113], v[208:211], v[54:57]
	v_mfma_i32_16x16x64_i8 v[46:49], v[98:101], v[216:219], v[46:49]
	v_mfma_i32_16x16x64_i8 v[38:41], v[110:113], v[216:219], v[38:41]
	v_mfma_i32_16x16x64_i8 v[30:33], v[98:101], v[224:227], v[30:33]
	v_mfma_i32_16x16x64_i8 v[22:25], v[110:113], v[224:227], v[22:25]
	v_mfma_i32_16x16x64_i8 v[14:17], v[98:101], v[232:235], v[14:17]
	v_mfma_i32_16x16x64_i8 v[6:9], v[110:113], v[232:235], v[6:9]
	s_setprio 0
	s_setprio 1
	v_mfma_i32_16x16x64_i8 v[58:61], v[188:191], v[204:207], v[58:61]
	v_mfma_i32_16x16x64_i8 v[50:53], v[196:199], v[204:207], v[50:53]
	v_mfma_i32_16x16x64_i8 v[42:45], v[188:191], v[212:215], v[42:45]
	v_mfma_i32_16x16x64_i8 v[34:37], v[196:199], v[212:215], v[34:37]
	v_mfma_i32_16x16x64_i8 v[26:29], v[188:191], v[220:223], v[26:29]
	v_mfma_i32_16x16x64_i8 v[18:21], v[196:199], v[220:223], v[18:21]
	v_mfma_i32_16x16x64_i8 v[10:13], v[188:191], v[228:231], v[10:13]
	v_mfma_i32_16x16x64_i8 v[2:5], v[196:199], v[228:231], v[2:5]
	v_mfma_i32_16x16x64_i8 v[58:61], v[192:195], v[208:211], v[58:61]
	v_mfma_i32_16x16x64_i8 v[50:53], v[200:203], v[208:211], v[50:53]
	v_mfma_i32_16x16x64_i8 v[42:45], v[192:195], v[216:219], v[42:45]
	v_mfma_i32_16x16x64_i8 v[34:37], v[200:203], v[216:219], v[34:37]
	v_mfma_i32_16x16x64_i8 v[26:29], v[192:195], v[224:227], v[26:29]
	v_mfma_i32_16x16x64_i8 v[18:21], v[200:203], v[224:227], v[18:21]
	v_mfma_i32_16x16x64_i8 v[10:13], v[192:195], v[232:235], v[10:13]
	v_mfma_i32_16x16x64_i8 v[2:5], v[200:203], v[232:235], v[2:5]
	s_setprio 0
	s_barrier
	s_add_i32 s55, 0, 0x18000
	s_add_i32 s56, 0, 0x1c000
	v_add_u32_e32 v110, s55, v185
	v_add_u32_e32 v184, s56, v185
	ds_read_b128 v[94:97], v110
	ds_read_b128 v[98:101], v110 offset:1024
	ds_read_b128 v[106:109], v110 offset:2048
	ds_read_b128 v[110:113], v110 offset:3072
	ds_read_b128 v[188:191], v184
	ds_read_b128 v[192:195], v184 offset:1024
	ds_read_b128 v[196:199], v184 offset:2048
	ds_read_b128 v[200:203], v184 offset:3072
	s_add_u32 s30, s30, 0x40000
	s_addc_u32 s31, s31, 0
	s_mov_b32 m0, s41
	v_lshl_add_u64 v[244:245], s[30:31], 0, v[146:147]
	ds_read_b128 v[204:207], v186 offset:32768
	ds_read_b128 v[208:211], v186 offset:33792
	ds_read_b128 v[212:215], v186 offset:34816
	ds_read_b128 v[216:219], v186 offset:35840
	ds_read_b128 v[220:223], v186 offset:36864
	ds_read_b128 v[224:227], v186 offset:37888
	ds_read_b128 v[228:231], v186 offset:38912
	ds_read_b128 v[232:235], v186 offset:39936
	global_load_lds_dwordx4 v[244:245], off
	v_lshl_add_u64 v[244:245], s[30:31], 0, v[150:151]
	s_mov_b32 m0, s42
	s_nop 0
	global_load_lds_dwordx4 v[244:245], off
	s_waitcnt vmcnt(8)
	s_waitcnt lgkmcnt(0)
	s_barrier
	s_setprio 1
	s_waitcnt lgkmcnt(0)
	v_mfma_i32_16x16x64_i8 v[142:145], v[94:97], v[204:207], v[142:145]
	v_mfma_i32_16x16x64_i8 v[134:137], v[106:109], v[204:207], v[134:137]
	v_mfma_i32_16x16x64_i8 v[126:129], v[94:97], v[212:215], v[126:129]
	v_mfma_i32_16x16x64_i8 v[118:121], v[106:109], v[212:215], v[118:121]
	v_mfma_i32_16x16x64_i8 v[102:105], v[94:97], v[220:223], v[102:105]
	v_mfma_i32_16x16x64_i8 v[86:89], v[106:109], v[220:223], v[86:89]
	v_mfma_i32_16x16x64_i8 v[78:81], v[94:97], v[228:231], v[78:81]
	v_mfma_i32_16x16x64_i8 v[70:73], v[106:109], v[228:231], v[70:73]
	v_mfma_i32_16x16x64_i8 v[142:145], v[98:101], v[208:211], v[142:145]
	v_mfma_i32_16x16x64_i8 v[134:137], v[110:113], v[208:211], v[134:137]
	v_mfma_i32_16x16x64_i8 v[126:129], v[98:101], v[216:219], v[126:129]
	v_mfma_i32_16x16x64_i8 v[118:121], v[110:113], v[216:219], v[118:121]
	v_mfma_i32_16x16x64_i8 v[102:105], v[98:101], v[224:227], v[102:105]
	v_mfma_i32_16x16x64_i8 v[86:89], v[110:113], v[224:227], v[86:89]
	v_mfma_i32_16x16x64_i8 v[78:81], v[98:101], v[232:235], v[78:81]
	v_mfma_i32_16x16x64_i8 v[70:73], v[110:113], v[232:235], v[70:73]
	s_setprio 0
	s_setprio 1
	v_mfma_i32_16x16x64_i8 v[138:141], v[188:191], v[204:207], v[138:141]
	v_mfma_i32_16x16x64_i8 v[130:133], v[196:199], v[204:207], v[130:133]
	v_mfma_i32_16x16x64_i8 v[122:125], v[188:191], v[212:215], v[122:125]
	v_mfma_i32_16x16x64_i8 v[114:117], v[196:199], v[212:215], v[114:117]
	v_mfma_i32_16x16x64_i8 v[90:93], v[188:191], v[220:223], v[90:93]
	v_mfma_i32_16x16x64_i8 v[82:85], v[196:199], v[220:223], v[82:85]
	v_mfma_i32_16x16x64_i8 v[74:77], v[188:191], v[228:231], v[74:77]
	v_mfma_i32_16x16x64_i8 v[66:69], v[196:199], v[228:231], v[66:69]
	v_mfma_i32_16x16x64_i8 v[138:141], v[192:195], v[208:211], v[138:141]
	v_mfma_i32_16x16x64_i8 v[130:133], v[200:203], v[208:211], v[130:133]
	v_mfma_i32_16x16x64_i8 v[122:125], v[192:195], v[216:219], v[122:125]
	v_mfma_i32_16x16x64_i8 v[114:117], v[200:203], v[216:219], v[114:117]
	v_mfma_i32_16x16x64_i8 v[90:93], v[192:195], v[224:227], v[90:93]
	v_mfma_i32_16x16x64_i8 v[82:85], v[200:203], v[224:227], v[82:85]
	v_mfma_i32_16x16x64_i8 v[74:77], v[192:195], v[232:235], v[74:77]
	v_mfma_i32_16x16x64_i8 v[66:69], v[200:203], v[232:235], v[66:69]
	s_setprio 0
	s_barrier
	s_add_i32 s30, s55, s37
	v_lshl_add_u64 v[236:237], v[236:237], 0, s[10:11]
	s_mov_b32 m0, s30
	ds_read_b128 v[204:207], v186 offset:49152
	ds_read_b128 v[208:211], v186 offset:50176
	ds_read_b128 v[212:215], v186 offset:51200
	ds_read_b128 v[216:219], v186 offset:52224
	ds_read_b128 v[220:223], v186 offset:53248
	ds_read_b128 v[224:227], v186 offset:54272
	ds_read_b128 v[228:231], v186 offset:55296
	ds_read_b128 v[232:235], v186 offset:56320
	global_load_lds_dwordx4 v[236:237], off
	s_add_i32 m0, s30, 0x2000
	s_add_u32 s28, s28, 0x40080
	v_lshl_add_u64 v[236:237], v[238:239], 0, s[10:11]
	s_addc_u32 s29, s29, 0
	s_add_i32 s30, s56, s37
	global_load_lds_dwordx4 v[236:237], off
	v_lshl_add_u64 v[236:237], s[28:29], 0, v[148:149]
	s_mov_b32 m0, s30
	s_nop 0
	global_load_lds_dwordx4 v[236:237], off
	v_lshl_add_u64 v[236:237], s[28:29], 0, v[152:153]
	s_add_i32 m0, s30, 0x2000
	s_nop 0
	global_load_lds_dwordx4 v[236:237], off
	v_lshl_add_u64 v[236:237], v[240:241], 0, s[10:11]
	s_mov_b32 m0, s45
	s_nop 0
	global_load_lds_dwordx4 v[236:237], off
	v_lshl_add_u64 v[236:237], v[242:243], 0, s[10:11]
	s_mov_b32 m0, s46
	s_nop 0
	global_load_lds_dwordx4 v[236:237], off
	s_waitcnt vmcnt(8)
	s_waitcnt lgkmcnt(0)
	s_barrier
	s_setprio 1
	s_waitcnt lgkmcnt(0)
	v_mfma_i32_16x16x64_i8 v[62:65], v[94:97], v[204:207], v[62:65]
	v_mfma_i32_16x16x64_i8 v[54:57], v[106:109], v[204:207], v[54:57]
	v_mfma_i32_16x16x64_i8 v[46:49], v[94:97], v[212:215], v[46:49]
	v_mfma_i32_16x16x64_i8 v[38:41], v[106:109], v[212:215], v[38:41]
	v_mfma_i32_16x16x64_i8 v[30:33], v[94:97], v[220:223], v[30:33]
	v_mfma_i32_16x16x64_i8 v[22:25], v[106:109], v[220:223], v[22:25]
	v_mfma_i32_16x16x64_i8 v[14:17], v[94:97], v[228:231], v[14:17]
	v_mfma_i32_16x16x64_i8 v[6:9], v[106:109], v[228:231], v[6:9]
	v_mfma_i32_16x16x64_i8 v[62:65], v[98:101], v[208:211], v[62:65]
	v_mfma_i32_16x16x64_i8 v[54:57], v[110:113], v[208:211], v[54:57]
	v_mfma_i32_16x16x64_i8 v[46:49], v[98:101], v[216:219], v[46:49]
	v_mfma_i32_16x16x64_i8 v[38:41], v[110:113], v[216:219], v[38:41]
	v_mfma_i32_16x16x64_i8 v[30:33], v[98:101], v[224:227], v[30:33]
	v_mfma_i32_16x16x64_i8 v[22:25], v[110:113], v[224:227], v[22:25]
	v_mfma_i32_16x16x64_i8 v[14:17], v[98:101], v[232:235], v[14:17]
	v_mfma_i32_16x16x64_i8 v[6:9], v[110:113], v[232:235], v[6:9]
	s_setprio 0
	s_setprio 1
	v_mfma_i32_16x16x64_i8 v[58:61], v[188:191], v[204:207], v[58:61]
	v_mfma_i32_16x16x64_i8 v[50:53], v[196:199], v[204:207], v[50:53]
	v_mfma_i32_16x16x64_i8 v[42:45], v[188:191], v[212:215], v[42:45]
	v_mfma_i32_16x16x64_i8 v[34:37], v[196:199], v[212:215], v[34:37]
	v_mfma_i32_16x16x64_i8 v[26:29], v[188:191], v[220:223], v[26:29]
	v_mfma_i32_16x16x64_i8 v[18:21], v[196:199], v[220:223], v[18:21]
	v_mfma_i32_16x16x64_i8 v[10:13], v[188:191], v[228:231], v[10:13]
	v_mfma_i32_16x16x64_i8 v[2:5], v[196:199], v[228:231], v[2:5]
	v_mfma_i32_16x16x64_i8 v[58:61], v[192:195], v[208:211], v[58:61]
	v_mfma_i32_16x16x64_i8 v[50:53], v[200:203], v[208:211], v[50:53]
	v_mfma_i32_16x16x64_i8 v[42:45], v[192:195], v[216:219], v[42:45]
	v_mfma_i32_16x16x64_i8 v[34:37], v[200:203], v[216:219], v[34:37]
	v_mfma_i32_16x16x64_i8 v[26:29], v[192:195], v[224:227], v[26:29]
	v_mfma_i32_16x16x64_i8 v[18:21], v[200:203], v[224:227], v[18:21]
	v_mfma_i32_16x16x64_i8 v[10:13], v[192:195], v[232:235], v[10:13]
	v_mfma_i32_16x16x64_i8 v[2:5], v[200:203], v[232:235], v[2:5]
	s_setprio 0
	s_barrier
	s_add_i32 s54, s54, 2
	s_add_u32 s26, s26, 0x100
	s_addc_u32 s27, s27, 0
	s_add_u32 s52, s52, 0x100
	s_addc_u32 s53, s53, 0
	s_cmp_gt_u32 s54, 13
	s_cbranch_scc0 .LBB0_1464
	s_and_b64 vcc, exec, s[12:13]
	s_cbranch_vccz .LBB0_1467
	s_barrier
.LBB0_1467:
	v_lshl_or_b32 v96, s25, 8, v156
	v_ashrrev_i32_e32 v97, 31, v96
	v_lshl_add_u64 v[96:97], v[96:97], 2, s[8:9]
	v_lshl_add_u32 v94, s24, 8, v154
	global_load_dwordx4 v[110:113], v[96:97], off
	v_ashrrev_i32_e32 v95, 31, v94
	v_lshl_add_u64 v[188:189], v[94:95], 2, s[4:5]
	global_load_dword v190, v[188:189], off
	global_load_dwordx4 v[106:109], v[96:97], off offset:512
	global_load_dwordx4 v[98:101], v[96:97], off offset:16
	s_nop 0
	global_load_dwordx4 v[94:97], v[96:97], off offset:528
	s_nop 0
	global_load_dword v184, v[188:189], off offset:64
	v_cvt_f32_i32_e32 v192, v138
	v_cvt_f32_i32_e32 v194, v140
	v_cvt_f32_i32_e32 v196, v134
	v_cvt_f32_i32_e32 v198, v130
	v_cvt_f32_i32_e32 v200, v136
	v_cvt_f32_i32_e32 v202, v132
	global_load_dword v140, v[188:189], off offset:128
	global_load_dword v138, v[188:189], off offset:192
	global_load_dword v136, v[188:189], off offset:512
	global_load_dword v134, v[188:189], off offset:576
	global_load_dword v132, v[188:189], off offset:640
	global_load_dword v130, v[188:189], off offset:704
	v_cvt_f32_i32_e32 v145, v145
	v_cvt_f32_i32_e32 v144, v144
	v_cvt_f32_i32_e32 v195, v141
	v_cvt_f32_i32_e32 v143, v143
	v_cvt_f32_i32_e32 v142, v142
	v_cvt_f32_i32_e32 v193, v139
	v_cvt_f32_i32_e32 v127, v127
	v_cvt_f32_i32_e32 v126, v126
	v_cvt_f32_i32_e32 v123, v123
	v_cvt_f32_i32_e32 v122, v122
	v_cvt_f32_i32_e32 v197, v135
	v_cvt_f32_i32_e32 v201, v137
	v_cvt_f32_i32_e32 v129, v129
	v_cvt_f32_i32_e32 v128, v128
	v_cvt_f32_i32_e32 v125, v125
	v_cvt_f32_i32_e32 v124, v124
	v_cvt_f32_i32_e32 v199, v131
	v_cvt_f32_i32_e32 v119, v119
	v_cvt_f32_i32_e32 v118, v118
	v_cvt_f32_i32_e32 v203, v133
	v_cvt_f32_i32_e32 v121, v121
	v_cvt_f32_i32_e32 v120, v120
	v_cvt_f32_i32_e32 v115, v115
	v_cvt_f32_i32_e32 v114, v114
	v_cvt_f32_i32_e32 v117, v117
	v_cvt_f32_i32_e32 v116, v116
	v_cvt_f32_i32_e32 v103, v103
	v_cvt_f32_i32_e32 v102, v102
	v_mov_b32_e32 v204, 0
	v_mov_b32_e32 v205, 0
	v_cvt_f32_i32_e32 v91, v91
	v_cvt_f32_i32_e32 v90, v90
	s_mul_i32 s17, s24, 44
	s_add_i32 s24, s17, s25
	s_ashr_i32 s25, s24, 31
	s_lshl_b64 s[24:25], s[24:25], 15
	v_cvt_f32_i32_e32 v105, v105
	v_cvt_f32_i32_e32 v104, v104
	v_cvt_f32_i32_e32 v93, v93
	v_cvt_f32_i32_e32 v92, v92
	v_cvt_f32_i32_e32 v87, v87
	v_cvt_f32_i32_e32 v86, v86
	v_cvt_f32_i32_e32 v89, v89
	v_cvt_f32_i32_e32 v88, v88
	v_cvt_f32_i32_e32 v83, v83
	v_cvt_f32_i32_e32 v82, v82
	v_cvt_f32_i32_e32 v85, v85
	v_cvt_f32_i32_e32 v84, v84
	v_cvt_f32_i32_e32 v79, v79
	v_cvt_f32_i32_e32 v78, v78
	v_cvt_f32_i32_e32 v75, v75
	v_cvt_f32_i32_e32 v74, v74
	v_cvt_f32_i32_e32 v81, v81
	v_cvt_f32_i32_e32 v80, v80
	v_cvt_f32_i32_e32 v77, v77
	v_cvt_f32_i32_e32 v76, v76
	v_cvt_f32_i32_e32 v71, v71
	v_cvt_f32_i32_e32 v70, v70
	v_cvt_f32_i32_e32 v73, v73
	v_cvt_f32_i32_e32 v72, v72
	v_cvt_f32_i32_e32 v67, v67
	v_cvt_f32_i32_e32 v66, v66
	v_cvt_f32_i32_e32 v69, v69
	v_cvt_f32_i32_e32 v68, v68
	v_cvt_f32_i32_e32 v63, v63
	v_cvt_f32_i32_e32 v62, v62
	v_cvt_f32_i32_e32 v59, v59
	v_cvt_f32_i32_e32 v58, v58
	v_cvt_f32_i32_e32 v65, v65
	s_waitcnt vmcnt(0)
	v_pk_mul_f32 v[188:189], v[112:113], v[190:191] op_sel_hi:[1,0]
	v_pk_mul_f32 v[208:209], v[108:109], v[190:191] op_sel_hi:[1,0]
	v_pk_mul_f32 v[144:145], v[188:189], v[144:145]
	v_pk_mul_f32 v[188:189], v[208:209], v[194:195]
	v_pk_mul_f32 v[206:207], v[110:111], v[190:191] op_sel_hi:[1,0]
	v_pk_mul_f32 v[188:189], v[144:145], v[188:189]
	v_pk_mul_f32 v[144:145], v[144:145], s[14:15] op_sel_hi:[1,0]
	v_pk_mul_f32 v[210:211], v[106:107], v[190:191] op_sel_hi:[1,0]
	v_exp_f32_e32 v144, v144
	v_exp_f32_e32 v145, v145
	v_pk_mul_f32 v[142:143], v[206:207], v[142:143]
	v_pk_mul_f32 v[192:193], v[210:211], v[192:193]
	v_pk_mul_f32 v[220:221], v[110:111], v[184:185] op_sel_hi:[1,0]
	v_pk_add_f32 v[144:145], v[144:145], 1.0 op_sel_hi:[1,0]
	v_pk_mul_f32 v[192:193], v[142:143], v[192:193]
	v_rcp_f32_e32 v144, v144
	v_rcp_f32_e32 v145, v145
	v_pk_mul_f32 v[142:143], v[142:143], s[14:15] op_sel_hi:[1,0]
	v_pk_mul_f32 v[126:127], v[220:221], v[126:127]
	v_exp_f32_e32 v142, v142
	v_exp_f32_e32 v143, v143
	v_pk_mul_f32 v[144:145], v[188:189], v[144:145]
	v_pk_mul_f32 v[218:219], v[112:113], v[184:185] op_sel_hi:[1,0]
	v_med3_f32 v135, v144, s49, v187
	v_med3_f32 v137, v145, s49, v187
	v_pk_mul_f32 v[144:145], v[106:107], v[184:185] op_sel_hi:[1,0]
	v_pk_add_f32 v[142:143], v[142:143], 1.0 op_sel_hi:[1,0]
	v_pk_mul_f32 v[122:123], v[144:145], v[122:123]
	v_pk_mul_f32 v[144:145], v[126:127], s[14:15] op_sel_hi:[1,0]
	v_rcp_f32_e32 v142, v142
	v_exp_f32_e32 v144, v144
	v_exp_f32_e32 v145, v145
	v_rcp_f32_e32 v143, v143
	v_pk_mul_f32 v[128:129], v[218:219], v[128:129]
	v_pk_mul_f32 v[122:123], v[126:127], v[122:123]
	v_pk_add_f32 v[126:127], v[144:145], 1.0 op_sel_hi:[1,0]
	v_pk_mul_f32 v[144:145], v[128:129], s[14:15] op_sel_hi:[1,0]
	v_pk_mul_f32 v[142:143], v[192:193], v[142:143]
	v_exp_f32_e32 v144, v144
	v_exp_f32_e32 v145, v145
	v_rcp_f32_e32 v126, v126
	v_rcp_f32_e32 v127, v127
	v_med3_f32 v131, v142, s49, v187
	v_med3_f32 v133, v143, s49, v187
	v_pk_mul_f32 v[142:143], v[108:109], v[184:185] op_sel_hi:[1,0]
	v_pk_mul_f32 v[212:213], v[100:101], v[190:191] op_sel_hi:[1,0]
	v_pk_mul_f32 v[124:125], v[142:143], v[124:125]
	v_pk_mul_f32 v[214:215], v[98:99], v[190:191] op_sel_hi:[1,0]
	v_pk_mul_f32 v[216:217], v[96:97], v[190:191] op_sel_hi:[1,0]
	v_pk_mul_f32 v[190:191], v[94:95], v[190:191] op_sel_hi:[1,0]
	v_pk_add_f32 v[144:145], v[144:145], 1.0 op_sel_hi:[1,0]
	v_pk_mul_f32 v[124:125], v[128:129], v[124:125]
	v_pk_mul_f32 v[128:129], v[98:99], v[184:185] op_sel_hi:[1,0]
	v_pk_mul_f32 v[194:195], v[214:215], v[196:197]
	v_pk_mul_f32 v[190:191], v[190:191], v[198:199]
	v_rcp_f32_e32 v144, v144
	v_rcp_f32_e32 v145, v145
	v_pk_mul_f32 v[122:123], v[122:123], v[126:127]
	v_pk_mul_f32 v[126:127], v[100:101], v[184:185] op_sel_hi:[1,0]
	v_pk_mul_f32 v[118:119], v[128:129], v[118:119]
	v_pk_mul_f32 v[190:191], v[194:195], v[190:191]
	v_pk_mul_f32 v[194:195], v[194:195], s[14:15] op_sel_hi:[1,0]
	v_pk_mul_f32 v[128:129], v[118:119], s[14:15] op_sel_hi:[1,0]
	v_pk_mul_f32 v[120:121], v[126:127], v[120:121]
	v_exp_f32_e32 v194, v194
	v_exp_f32_e32 v195, v195
	v_exp_f32_e32 v128, v128
	v_exp_f32_e32 v129, v129
	v_pk_mul_f32 v[126:127], v[120:121], s[14:15] op_sel_hi:[1,0]
	v_pk_mul_f32 v[196:197], v[212:213], v[200:201]
	v_exp_f32_e32 v126, v126
	v_exp_f32_e32 v127, v127
	v_pk_mul_f32 v[198:199], v[216:217], v[202:203]
	v_pk_mul_f32 v[124:125], v[124:125], v[144:145]
	v_pk_mul_f32 v[144:145], v[94:95], v[184:185] op_sel_hi:[1,0]
	v_pk_mul_f32 v[198:199], v[196:197], v[198:199]
	v_pk_mul_f32 v[196:197], v[196:197], s[14:15] op_sel_hi:[1,0]
	v_pk_mul_f32 v[114:115], v[144:145], v[114:115]
	v_exp_f32_e32 v196, v196
	v_exp_f32_e32 v197, v197
	v_pk_add_f32 v[194:195], v[194:195], 1.0 op_sel_hi:[1,0]
	v_pk_mul_f32 v[114:115], v[118:119], v[114:115]
	v_pk_add_f32 v[118:119], v[128:129], 1.0 op_sel_hi:[1,0]
	v_rcp_f32_e32 v194, v194
	v_rcp_f32_e32 v195, v195
	v_rcp_f32_e32 v118, v118
	v_rcp_f32_e32 v119, v119
	v_pk_add_f32 v[126:127], v[126:127], 1.0 op_sel_hi:[1,0]
	v_pk_mul_f32 v[142:143], v[96:97], v[184:185] op_sel_hi:[1,0]
	v_rcp_f32_e32 v126, v126
	v_rcp_f32_e32 v127, v127
	v_pk_add_f32 v[196:197], v[196:197], 1.0 op_sel_hi:[1,0]
	v_pk_mul_f32 v[116:117], v[142:143], v[116:117]
	v_rcp_f32_e32 v196, v196
	v_rcp_f32_e32 v197, v197
	v_pk_mul_f32 v[188:189], v[190:191], v[194:195]
	v_pk_mul_f32 v[114:115], v[114:115], v[118:119]
	v_pk_mul_f32 v[116:117], v[120:121], v[116:117]
	v_med3_f32 v119, v122, s49, v187
	v_med3_f32 v120, v123, s49, v187
	v_mov_b32_e32 v118, 0
	v_med3_f32 v139, v188, s49, v187
	v_med3_f32 v141, v189, s49, v187
	v_pk_mul_f32 v[116:117], v[116:117], v[126:127]
	v_cvt_pk_fp8_f32 v118, v119, v120
	v_med3_f32 v114, v114, s49, v187
	v_med3_f32 v115, v115, s49, v187
	v_mov_b32_e32 v119, 0
	v_cvt_pk_fp8_f32 v204, v131, v133
	v_cvt_pk_fp8_f32 v205, v139, v141
	v_cvt_pk_fp8_f32 v119, v114, v115
	v_med3_f32 v114, v116, s49, v187
	v_med3_f32 v115, v117, s49, v187
	v_pk_mul_f32 v[116:117], v[110:111], v[140:141] op_sel_hi:[1,0]
	v_pk_mul_f32 v[190:191], v[198:199], v[196:197]
	v_pk_mul_f32 v[102:103], v[116:117], v[102:103]
	v_med3_f32 v131, v190, s49, v187
	v_pk_mul_f32 v[116:117], v[102:103], s[14:15] op_sel_hi:[1,0]
	v_med3_f32 v133, v191, s49, v187
	v_exp_f32_e32 v116, v116
	v_exp_f32_e32 v117, v117
	v_cvt_pk_fp8_f32 v204, v135, v137 op_sel:[0,0,1]
	v_cvt_pk_fp8_f32 v205, v131, v133 op_sel:[0,0,1]
	v_med3_f32 v121, v124, s49, v187
	v_med3_f32 v122, v125, s49, v187
	v_cvt_pk_fp8_f32 v118, v121, v122 op_sel:[0,0,1]
	v_cvt_pk_fp8_f32 v119, v114, v115 op_sel:[0,0,1]
	v_pk_mul_f32 v[120:121], v[106:107], v[140:141] op_sel_hi:[1,0]
	v_lshl_add_u64 v[114:115], v[158:159], 0, s[24:25]
	v_pk_mul_f32 v[90:91], v[120:121], v[90:91]
	global_store_dwordx2 v[114:115], v[204:205], off
	v_pk_mul_f32 v[90:91], v[102:103], v[90:91]
	v_pk_add_f32 v[102:103], v[116:117], 1.0 op_sel_hi:[1,0]
	v_lshl_add_u64 v[114:115], v[160:161], 0, s[24:25]
	v_rcp_f32_e32 v102, v102
	v_rcp_f32_e32 v103, v103
	global_store_dwordx2 v[114:115], v[118:119], off
	v_pk_mul_f32 v[114:115], v[112:113], v[140:141] op_sel_hi:[1,0]
	v_pk_mul_f32 v[118:119], v[108:109], v[140:141] op_sel_hi:[1,0]
	v_pk_mul_f32 v[104:105], v[114:115], v[104:105]
	v_pk_mul_f32 v[92:93], v[118:119], v[92:93]
	v_pk_mul_f32 v[114:115], v[104:105], s[14:15] op_sel_hi:[1,0]
	v_pk_mul_f32 v[92:93], v[104:105], v[92:93]
	v_pk_mul_f32 v[104:105], v[98:99], v[140:141] op_sel_hi:[1,0]
	v_exp_f32_e32 v114, v114
	v_exp_f32_e32 v115, v115
	v_pk_mul_f32 v[90:91], v[90:91], v[102:103]
	v_pk_mul_f32 v[102:103], v[100:101], v[140:141] op_sel_hi:[1,0]
	v_pk_mul_f32 v[86:87], v[104:105], v[86:87]
	v_pk_mul_f32 v[88:89], v[102:103], v[88:89]
	v_pk_mul_f32 v[104:105], v[86:87], s[14:15] op_sel_hi:[1,0]
	v_pk_mul_f32 v[102:103], v[88:89], s[14:15] op_sel_hi:[1,0]
	v_exp_f32_e32 v104, v104
	v_exp_f32_e32 v105, v105
	v_exp_f32_e32 v102, v102
	v_exp_f32_e32 v103, v103
	v_pk_add_f32 v[114:115], v[114:115], 1.0 op_sel_hi:[1,0]
	v_pk_mul_f32 v[116:117], v[94:95], v[140:141] op_sel_hi:[1,0]
	v_rcp_f32_e32 v114, v114
	v_rcp_f32_e32 v115, v115
	v_pk_mul_f32 v[82:83], v[116:117], v[82:83]
	v_pk_add_f32 v[102:103], v[102:103], 1.0 op_sel_hi:[1,0]
	v_pk_mul_f32 v[82:83], v[86:87], v[82:83]
	v_pk_add_f32 v[86:87], v[104:105], 1.0 op_sel_hi:[1,0]
	v_rcp_f32_e32 v102, v102
	v_rcp_f32_e32 v86, v86
	v_rcp_f32_e32 v87, v87
	v_rcp_f32_e32 v103, v103
	v_pk_mul_f32 v[92:93], v[92:93], v[114:115]
	v_pk_mul_f32 v[114:115], v[96:97], v[140:141] op_sel_hi:[1,0]
	v_pk_mul_f32 v[82:83], v[82:83], v[86:87]
	v_pk_mul_f32 v[84:85], v[114:115], v[84:85]
	v_med3_f32 v87, v90, s49, v187
	v_pk_mul_f32 v[84:85], v[88:89], v[84:85]
	v_med3_f32 v88, v91, s49, v187
	v_mov_b32_e32 v86, 0
	v_pk_mul_f32 v[84:85], v[84:85], v[102:103]
	v_cvt_pk_fp8_f32 v86, v87, v88
	v_med3_f32 v82, v82, s49, v187
	v_med3_f32 v83, v83, s49, v187
	v_mov_b32_e32 v87, 0
	v_cvt_pk_fp8_f32 v87, v82, v83
	v_med3_f32 v82, v84, s49, v187
	v_med3_f32 v83, v85, s49, v187
	v_pk_mul_f32 v[84:85], v[110:111], v[138:139] op_sel_hi:[1,0]
	v_med3_f32 v89, v92, s49, v187
	v_pk_mul_f32 v[78:79], v[84:85], v[78:79]
	v_med3_f32 v90, v93, s49, v187
	v_pk_mul_f32 v[84:85], v[78:79], s[14:15] op_sel_hi:[1,0]
	v_cvt_pk_fp8_f32 v86, v89, v90 op_sel:[0,0,1]
	v_exp_f32_e32 v84, v84
	v_exp_f32_e32 v85, v85
	v_pk_mul_f32 v[90:91], v[106:107], v[138:139] op_sel_hi:[1,0]
	v_cvt_pk_fp8_f32 v87, v82, v83 op_sel:[0,0,1]
	v_pk_mul_f32 v[74:75], v[90:91], v[74:75]
	v_pk_mul_f32 v[82:83], v[112:113], v[138:139] op_sel_hi:[1,0]
	v_pk_mul_f32 v[74:75], v[78:79], v[74:75]
	v_pk_add_f32 v[78:79], v[84:85], 1.0 op_sel_hi:[1,0]
	v_pk_mul_f32 v[88:89], v[108:109], v[138:139] op_sel_hi:[1,0]
	v_rcp_f32_e32 v78, v78
	v_rcp_f32_e32 v79, v79
	v_pk_mul_f32 v[80:81], v[82:83], v[80:81]
	v_pk_mul_f32 v[76:77], v[88:89], v[76:77]
	v_pk_mul_f32 v[82:83], v[80:81], s[14:15] op_sel_hi:[1,0]
	v_pk_mul_f32 v[76:77], v[80:81], v[76:77]
	v_pk_mul_f32 v[80:81], v[98:99], v[138:139] op_sel_hi:[1,0]
	v_exp_f32_e32 v82, v82
	v_exp_f32_e32 v83, v83
	v_pk_mul_f32 v[74:75], v[74:75], v[78:79]
	v_pk_mul_f32 v[78:79], v[100:101], v[138:139] op_sel_hi:[1,0]
	v_pk_mul_f32 v[70:71], v[80:81], v[70:71]
	v_pk_mul_f32 v[72:73], v[78:79], v[72:73]
	v_pk_mul_f32 v[80:81], v[70:71], s[14:15] op_sel_hi:[1,0]
	v_pk_mul_f32 v[78:79], v[72:73], s[14:15] op_sel_hi:[1,0]
	v_exp_f32_e32 v80, v80
	v_exp_f32_e32 v81, v81
	v_exp_f32_e32 v78, v78
	v_exp_f32_e32 v79, v79
	v_pk_add_f32 v[82:83], v[82:83], 1.0 op_sel_hi:[1,0]
	v_pk_mul_f32 v[84:85], v[94:95], v[138:139] op_sel_hi:[1,0]
	v_rcp_f32_e32 v82, v82
	v_rcp_f32_e32 v83, v83
	v_pk_mul_f32 v[66:67], v[84:85], v[66:67]
	v_pk_add_f32 v[78:79], v[78:79], 1.0 op_sel_hi:[1,0]
	v_pk_mul_f32 v[66:67], v[70:71], v[66:67]
	v_pk_add_f32 v[70:71], v[80:81], 1.0 op_sel_hi:[1,0]
	v_rcp_f32_e32 v78, v78
	v_rcp_f32_e32 v70, v70
	v_rcp_f32_e32 v71, v71
	v_rcp_f32_e32 v79, v79
	v_pk_mul_f32 v[76:77], v[76:77], v[82:83]
	v_pk_mul_f32 v[82:83], v[96:97], v[138:139] op_sel_hi:[1,0]
	v_pk_mul_f32 v[66:67], v[66:67], v[70:71]
	v_pk_mul_f32 v[68:69], v[82:83], v[68:69]
	v_med3_f32 v71, v74, s49, v187
	v_pk_mul_f32 v[68:69], v[72:73], v[68:69]
	v_med3_f32 v72, v75, s49, v187
	v_mov_b32_e32 v70, 0
	v_pk_mul_f32 v[68:69], v[68:69], v[78:79]
	v_cvt_pk_fp8_f32 v70, v71, v72
	v_med3_f32 v66, v66, s49, v187
	v_med3_f32 v67, v67, s49, v187
	v_mov_b32_e32 v71, 0
	v_cvt_pk_fp8_f32 v71, v66, v67
	v_med3_f32 v66, v68, s49, v187
	v_med3_f32 v67, v69, s49, v187
	v_pk_mul_f32 v[68:69], v[110:111], v[136:137] op_sel_hi:[1,0]
	v_med3_f32 v73, v76, s49, v187
	v_pk_mul_f32 v[62:63], v[68:69], v[62:63]
	v_med3_f32 v74, v77, s49, v187
	v_pk_mul_f32 v[68:69], v[62:63], s[14:15] op_sel_hi:[1,0]
	v_cvt_pk_fp8_f32 v70, v73, v74 op_sel:[0,0,1]
	v_exp_f32_e32 v68, v68
	v_exp_f32_e32 v69, v69
	v_cvt_pk_fp8_f32 v71, v66, v67 op_sel:[0,0,1]
	v_pk_mul_f32 v[72:73], v[106:107], v[136:137] op_sel_hi:[1,0]
	v_cvt_f32_i32_e32 v64, v64
	v_pk_mul_f32 v[58:59], v[72:73], v[58:59]
	v_cvt_f32_i32_e32 v61, v61
	v_cvt_f32_i32_e32 v60, v60
	v_lshl_add_u64 v[66:67], v[164:165], 0, s[24:25]
	v_pk_mul_f32 v[58:59], v[62:63], v[58:59]
	v_pk_add_f32 v[62:63], v[68:69], 1.0 op_sel_hi:[1,0]
	global_store_dwordx2 v[66:67], v[86:87], off
	v_lshl_add_u64 v[66:67], v[166:167], 0, s[24:25]
	v_rcp_f32_e32 v62, v62
	v_rcp_f32_e32 v63, v63
	v_cvt_f32_i32_e32 v55, v55
	v_cvt_f32_i32_e32 v54, v54
	global_store_dwordx2 v[66:67], v[70:71], off
	v_pk_mul_f32 v[66:67], v[112:113], v[136:137] op_sel_hi:[1,0]
	v_pk_mul_f32 v[70:71], v[108:109], v[136:137] op_sel_hi:[1,0]
	v_cvt_f32_i32_e32 v57, v57
	v_cvt_f32_i32_e32 v56, v56
	v_pk_mul_f32 v[64:65], v[66:67], v[64:65]
	v_pk_mul_f32 v[60:61], v[70:71], v[60:61]
	v_pk_mul_f32 v[66:67], v[64:65], s[14:15] op_sel_hi:[1,0]
	v_pk_mul_f32 v[60:61], v[64:65], v[60:61]
	v_pk_mul_f32 v[64:65], v[98:99], v[136:137] op_sel_hi:[1,0]
	v_exp_f32_e32 v66, v66
	v_exp_f32_e32 v67, v67
	v_pk_mul_f32 v[58:59], v[58:59], v[62:63]
	v_pk_mul_f32 v[62:63], v[100:101], v[136:137] op_sel_hi:[1,0]
	v_pk_mul_f32 v[54:55], v[64:65], v[54:55]
	v_cvt_f32_i32_e32 v51, v51
	v_cvt_f32_i32_e32 v50, v50
	v_pk_mul_f32 v[64:65], v[54:55], s[14:15] op_sel_hi:[1,0]
	v_pk_mul_f32 v[56:57], v[62:63], v[56:57]
	v_exp_f32_e32 v64, v64
	v_exp_f32_e32 v65, v65
	v_pk_mul_f32 v[62:63], v[56:57], s[14:15] op_sel_hi:[1,0]
	v_pk_add_f32 v[66:67], v[66:67], 1.0 op_sel_hi:[1,0]
	v_exp_f32_e32 v62, v62
	v_exp_f32_e32 v63, v63
	v_pk_mul_f32 v[68:69], v[94:95], v[136:137] op_sel_hi:[1,0]
	v_rcp_f32_e32 v66, v66
	v_rcp_f32_e32 v67, v67
	v_pk_mul_f32 v[50:51], v[68:69], v[50:51]
	v_cvt_f32_i32_e32 v53, v53
	v_pk_mul_f32 v[50:51], v[54:55], v[50:51]
	v_pk_add_f32 v[54:55], v[64:65], 1.0 op_sel_hi:[1,0]
	v_cvt_f32_i32_e32 v52, v52
	v_rcp_f32_e32 v54, v54
	v_rcp_f32_e32 v55, v55
	v_pk_add_f32 v[62:63], v[62:63], 1.0 op_sel_hi:[1,0]
	v_pk_mul_f32 v[60:61], v[60:61], v[66:67]
	v_rcp_f32_e32 v62, v62
	v_rcp_f32_e32 v63, v63
	v_pk_mul_f32 v[66:67], v[96:97], v[136:137] op_sel_hi:[1,0]
	v_cvt_f32_i32_e32 v47, v47
	v_pk_mul_f32 v[52:53], v[66:67], v[52:53]
	v_cvt_f32_i32_e32 v46, v46
	v_pk_mul_f32 v[50:51], v[50:51], v[54:55]
	v_pk_mul_f32 v[52:53], v[56:57], v[52:53]
	v_med3_f32 v55, v58, s49, v187
	v_med3_f32 v56, v59, s49, v187
	v_mov_b32_e32 v54, 0
	v_pk_mul_f32 v[52:53], v[52:53], v[62:63]
	v_cvt_pk_fp8_f32 v54, v55, v56
	v_med3_f32 v50, v50, s49, v187
	v_med3_f32 v51, v51, s49, v187
	v_mov_b32_e32 v55, 0
	v_cvt_pk_fp8_f32 v55, v50, v51
	v_med3_f32 v50, v52, s49, v187
	v_med3_f32 v51, v53, s49, v187
	v_pk_mul_f32 v[52:53], v[110:111], v[134:135] op_sel_hi:[1,0]
	v_cvt_f32_i32_e32 v43, v43
	v_pk_mul_f32 v[46:47], v[52:53], v[46:47]
	v_cvt_f32_i32_e32 v42, v42
	v_pk_mul_f32 v[52:53], v[46:47], s[14:15] op_sel_hi:[1,0]
	v_med3_f32 v57, v60, s49, v187
	v_exp_f32_e32 v52, v52
	v_exp_f32_e32 v53, v53
	v_med3_f32 v58, v61, s49, v187
	v_cvt_pk_fp8_f32 v54, v57, v58 op_sel:[0,0,1]
	v_pk_mul_f32 v[58:59], v[106:107], v[134:135] op_sel_hi:[1,0]
	v_cvt_f32_i32_e32 v49, v49
	v_pk_mul_f32 v[42:43], v[58:59], v[42:43]
	v_cvt_f32_i32_e32 v48, v48
	v_cvt_f32_i32_e32 v45, v45
	v_cvt_f32_i32_e32 v44, v44
	v_pk_mul_f32 v[42:43], v[46:47], v[42:43]
	v_pk_add_f32 v[46:47], v[52:53], 1.0 op_sel_hi:[1,0]
	v_cvt_f32_i32_e32 v39, v39
	v_rcp_f32_e32 v46, v46
	v_rcp_f32_e32 v47, v47
	v_cvt_f32_i32_e32 v38, v38
	v_cvt_pk_fp8_f32 v55, v50, v51 op_sel:[0,0,1]
	v_pk_mul_f32 v[50:51], v[112:113], v[134:135] op_sel_hi:[1,0]
	v_pk_mul_f32 v[56:57], v[108:109], v[134:135] op_sel_hi:[1,0]
	v_cvt_f32_i32_e32 v41, v41
	v_cvt_f32_i32_e32 v40, v40
	v_pk_mul_f32 v[48:49], v[50:51], v[48:49]
	v_pk_mul_f32 v[44:45], v[56:57], v[44:45]
	v_pk_mul_f32 v[50:51], v[48:49], s[14:15] op_sel_hi:[1,0]
	v_pk_mul_f32 v[44:45], v[48:49], v[44:45]
	v_pk_mul_f32 v[48:49], v[98:99], v[134:135] op_sel_hi:[1,0]
	v_exp_f32_e32 v50, v50
	v_exp_f32_e32 v51, v51
	v_pk_mul_f32 v[42:43], v[42:43], v[46:47]
	v_pk_mul_f32 v[46:47], v[100:101], v[134:135] op_sel_hi:[1,0]
	v_pk_mul_f32 v[38:39], v[48:49], v[38:39]
	v_cvt_f32_i32_e32 v35, v35
	v_cvt_f32_i32_e32 v34, v34
	v_pk_mul_f32 v[48:49], v[38:39], s[14:15] op_sel_hi:[1,0]
	v_pk_mul_f32 v[40:41], v[46:47], v[40:41]
	v_exp_f32_e32 v48, v48
	v_exp_f32_e32 v49, v49
	v_pk_mul_f32 v[46:47], v[40:41], s[14:15] op_sel_hi:[1,0]
	v_pk_add_f32 v[50:51], v[50:51], 1.0 op_sel_hi:[1,0]
	v_exp_f32_e32 v46, v46
	v_exp_f32_e32 v47, v47
	v_pk_mul_f32 v[52:53], v[94:95], v[134:135] op_sel_hi:[1,0]
	v_rcp_f32_e32 v50, v50
	v_rcp_f32_e32 v51, v51
	v_pk_mul_f32 v[34:35], v[52:53], v[34:35]
	v_cvt_f32_i32_e32 v37, v37
	v_pk_mul_f32 v[34:35], v[38:39], v[34:35]
	v_pk_add_f32 v[38:39], v[48:49], 1.0 op_sel_hi:[1,0]
	v_cvt_f32_i32_e32 v36, v36
	v_rcp_f32_e32 v38, v38
	v_rcp_f32_e32 v39, v39
	v_pk_add_f32 v[46:47], v[46:47], 1.0 op_sel_hi:[1,0]
	v_pk_mul_f32 v[44:45], v[44:45], v[50:51]
	v_rcp_f32_e32 v46, v46
	v_rcp_f32_e32 v47, v47
	v_pk_mul_f32 v[50:51], v[96:97], v[134:135] op_sel_hi:[1,0]
	v_cvt_f32_i32_e32 v31, v31
	v_pk_mul_f32 v[36:37], v[50:51], v[36:37]
	v_cvt_f32_i32_e32 v30, v30
	v_pk_mul_f32 v[34:35], v[34:35], v[38:39]
	v_pk_mul_f32 v[36:37], v[40:41], v[36:37]
	v_med3_f32 v39, v42, s49, v187
	v_med3_f32 v40, v43, s49, v187
	v_mov_b32_e32 v38, 0
	v_pk_mul_f32 v[36:37], v[36:37], v[46:47]
	v_cvt_pk_fp8_f32 v38, v39, v40
	v_med3_f32 v34, v34, s49, v187
	v_med3_f32 v35, v35, s49, v187
	v_mov_b32_e32 v39, 0
	v_cvt_pk_fp8_f32 v39, v34, v35
	v_med3_f32 v34, v36, s49, v187
	v_med3_f32 v35, v37, s49, v187
	v_pk_mul_f32 v[36:37], v[110:111], v[132:133] op_sel_hi:[1,0]
	v_cvt_f32_i32_e32 v27, v27
	v_pk_mul_f32 v[30:31], v[36:37], v[30:31]
	v_cvt_f32_i32_e32 v26, v26
	v_pk_mul_f32 v[36:37], v[30:31], s[14:15] op_sel_hi:[1,0]
	v_med3_f32 v41, v44, s49, v187
	v_exp_f32_e32 v36, v36
	v_exp_f32_e32 v37, v37
	v_med3_f32 v42, v45, s49, v187
	v_cvt_pk_fp8_f32 v38, v41, v42 op_sel:[0,0,1]
	v_cvt_pk_fp8_f32 v39, v34, v35 op_sel:[0,0,1]
	v_pk_mul_f32 v[40:41], v[106:107], v[132:133] op_sel_hi:[1,0]
	v_cvt_f32_i32_e32 v33, v33
	v_pk_mul_f32 v[26:27], v[40:41], v[26:27]
	v_cvt_f32_i32_e32 v32, v32
	v_cvt_f32_i32_e32 v29, v29
	v_cvt_f32_i32_e32 v28, v28
	v_lshl_add_u64 v[34:35], v[168:169], 0, s[24:25]
	v_pk_mul_f32 v[26:27], v[30:31], v[26:27]
	v_pk_add_f32 v[30:31], v[36:37], 1.0 op_sel_hi:[1,0]
	global_store_dwordx2 v[34:35], v[54:55], off
	v_lshl_add_u64 v[34:35], v[170:171], 0, s[24:25]
	v_rcp_f32_e32 v30, v30
	v_rcp_f32_e32 v31, v31
	v_cvt_f32_i32_e32 v23, v23
	v_cvt_f32_i32_e32 v22, v22
	global_store_dwordx2 v[34:35], v[38:39], off
	v_pk_mul_f32 v[34:35], v[112:113], v[132:133] op_sel_hi:[1,0]
	v_pk_mul_f32 v[38:39], v[108:109], v[132:133] op_sel_hi:[1,0]
	v_cvt_f32_i32_e32 v25, v25
	v_cvt_f32_i32_e32 v24, v24
	v_pk_mul_f32 v[32:33], v[34:35], v[32:33]
	v_pk_mul_f32 v[28:29], v[38:39], v[28:29]
	v_pk_mul_f32 v[34:35], v[32:33], s[14:15] op_sel_hi:[1,0]
	v_pk_mul_f32 v[28:29], v[32:33], v[28:29]
	v_pk_mul_f32 v[32:33], v[98:99], v[132:133] op_sel_hi:[1,0]
	v_exp_f32_e32 v34, v34
	v_exp_f32_e32 v35, v35
	v_pk_mul_f32 v[26:27], v[26:27], v[30:31]
	v_pk_mul_f32 v[30:31], v[100:101], v[132:133] op_sel_hi:[1,0]
	v_pk_mul_f32 v[22:23], v[32:33], v[22:23]
	v_cvt_f32_i32_e32 v19, v19
	v_cvt_f32_i32_e32 v18, v18
	v_pk_mul_f32 v[32:33], v[22:23], s[14:15] op_sel_hi:[1,0]
	v_pk_mul_f32 v[24:25], v[30:31], v[24:25]
	v_exp_f32_e32 v32, v32
	v_exp_f32_e32 v33, v33
	v_pk_mul_f32 v[30:31], v[24:25], s[14:15] op_sel_hi:[1,0]
	v_pk_add_f32 v[34:35], v[34:35], 1.0 op_sel_hi:[1,0]
	v_exp_f32_e32 v30, v30
	v_exp_f32_e32 v31, v31
	v_pk_mul_f32 v[36:37], v[94:95], v[132:133] op_sel_hi:[1,0]
	v_rcp_f32_e32 v34, v34
	v_rcp_f32_e32 v35, v35
	v_pk_mul_f32 v[18:19], v[36:37], v[18:19]
	v_cvt_f32_i32_e32 v21, v21
	v_pk_mul_f32 v[18:19], v[22:23], v[18:19]
	v_pk_add_f32 v[22:23], v[32:33], 1.0 op_sel_hi:[1,0]
	v_cvt_f32_i32_e32 v20, v20
	v_rcp_f32_e32 v22, v22
	v_rcp_f32_e32 v23, v23
	v_pk_add_f32 v[30:31], v[30:31], 1.0 op_sel_hi:[1,0]
	v_pk_mul_f32 v[28:29], v[28:29], v[34:35]
	v_rcp_f32_e32 v30, v30
	v_rcp_f32_e32 v31, v31
	v_pk_mul_f32 v[34:35], v[96:97], v[132:133] op_sel_hi:[1,0]
	v_cvt_f32_i32_e32 v15, v15
	v_pk_mul_f32 v[20:21], v[34:35], v[20:21]
	v_cvt_f32_i32_e32 v14, v14
	v_pk_mul_f32 v[18:19], v[18:19], v[22:23]
	v_pk_mul_f32 v[20:21], v[24:25], v[20:21]
	v_med3_f32 v23, v26, s49, v187
	v_med3_f32 v24, v27, s49, v187
	v_mov_b32_e32 v22, 0
	v_pk_mul_f32 v[20:21], v[20:21], v[30:31]
	v_cvt_pk_fp8_f32 v22, v23, v24
	v_med3_f32 v18, v18, s49, v187
	v_med3_f32 v19, v19, s49, v187
	v_mov_b32_e32 v23, 0
	v_cvt_pk_fp8_f32 v23, v18, v19
	v_med3_f32 v18, v20, s49, v187
	v_med3_f32 v19, v21, s49, v187
	v_pk_mul_f32 v[20:21], v[110:111], v[130:131] op_sel_hi:[1,0]
	v_cvt_f32_i32_e32 v11, v11
	v_pk_mul_f32 v[14:15], v[20:21], v[14:15]
	v_cvt_f32_i32_e32 v10, v10
	v_pk_mul_f32 v[20:21], v[14:15], s[14:15] op_sel_hi:[1,0]
	v_cvt_f32_i32_e32 v17, v17
	v_exp_f32_e32 v20, v20
	v_exp_f32_e32 v21, v21
	v_cvt_f32_i32_e32 v16, v16
	v_cvt_f32_i32_e32 v13, v13
	v_cvt_f32_i32_e32 v12, v12
	v_med3_f32 v25, v28, s49, v187
	v_med3_f32 v26, v29, s49, v187
	v_cvt_pk_fp8_f32 v22, v25, v26 op_sel:[0,0,1]
	v_pk_mul_f32 v[26:27], v[106:107], v[130:131] op_sel_hi:[1,0]
	v_cvt_f32_i32_e32 v7, v7
	v_cvt_f32_i32_e32 v6, v6
	v_cvt_pk_fp8_f32 v23, v18, v19 op_sel:[0,0,1]
	v_pk_mul_f32 v[18:19], v[112:113], v[130:131] op_sel_hi:[1,0]
	v_pk_mul_f32 v[24:25], v[108:109], v[130:131] op_sel_hi:[1,0]
	v_pk_mul_f32 v[10:11], v[26:27], v[10:11]
	v_pk_mul_f32 v[16:17], v[18:19], v[16:17]
	v_pk_mul_f32 v[10:11], v[14:15], v[10:11]
	v_pk_add_f32 v[14:15], v[20:21], 1.0 op_sel_hi:[1,0]
	v_pk_mul_f32 v[12:13], v[24:25], v[12:13]
	v_rcp_f32_e32 v14, v14
	v_pk_mul_f32 v[18:19], v[16:17], s[14:15] op_sel_hi:[1,0]
	v_rcp_f32_e32 v15, v15
	v_pk_mul_f32 v[12:13], v[16:17], v[12:13]
	v_pk_mul_f32 v[16:17], v[98:99], v[130:131] op_sel_hi:[1,0]
	v_exp_f32_e32 v18, v18
	v_exp_f32_e32 v19, v19
	v_pk_mul_f32 v[6:7], v[16:17], v[6:7]
	v_cvt_f32_i32_e32 v9, v9
	v_cvt_f32_i32_e32 v8, v8
	v_cvt_f32_i32_e32 v3, v3
	v_cvt_f32_i32_e32 v2, v2
	v_pk_mul_f32 v[16:17], v[6:7], s[14:15] op_sel_hi:[1,0]
	v_pk_mul_f32 v[10:11], v[10:11], v[14:15]
	v_exp_f32_e32 v16, v16
	v_exp_f32_e32 v17, v17
	v_pk_mul_f32 v[14:15], v[100:101], v[130:131] op_sel_hi:[1,0]
	v_pk_add_f32 v[18:19], v[18:19], 1.0 op_sel_hi:[1,0]
	v_pk_mul_f32 v[20:21], v[94:95], v[130:131] op_sel_hi:[1,0]
	v_pk_mul_f32 v[8:9], v[14:15], v[8:9]
	v_rcp_f32_e32 v18, v18
	v_rcp_f32_e32 v19, v19
	v_pk_mul_f32 v[2:3], v[20:21], v[2:3]
	v_pk_mul_f32 v[14:15], v[8:9], s[14:15] op_sel_hi:[1,0]
	v_pk_mul_f32 v[2:3], v[6:7], v[2:3]
	v_pk_add_f32 v[6:7], v[16:17], 1.0 op_sel_hi:[1,0]
	v_exp_f32_e32 v14, v14
	v_exp_f32_e32 v15, v15
	v_cvt_f32_i32_e32 v5, v5
	v_cvt_f32_i32_e32 v4, v4
	v_rcp_f32_e32 v6, v6
	v_rcp_f32_e32 v7, v7
	v_pk_mul_f32 v[12:13], v[12:13], v[18:19]
	v_pk_mul_f32 v[18:19], v[96:97], v[130:131] op_sel_hi:[1,0]
	v_pk_add_f32 v[14:15], v[14:15], 1.0 op_sel_hi:[1,0]
	v_pk_mul_f32 v[4:5], v[18:19], v[4:5]
	v_rcp_f32_e32 v14, v14
	v_rcp_f32_e32 v15, v15
	v_pk_mul_f32 v[2:3], v[2:3], v[6:7]
	v_pk_mul_f32 v[4:5], v[8:9], v[4:5]
	v_med3_f32 v7, v10, s49, v187
	v_med3_f32 v8, v11, s49, v187
	v_mov_b32_e32 v6, 0
	v_cvt_pk_fp8_f32 v6, v7, v8
	v_med3_f32 v2, v2, s49, v187
	v_med3_f32 v3, v3, s49, v187
	v_mov_b32_e32 v7, 0
	v_cvt_pk_fp8_f32 v7, v2, v3
	v_pk_mul_f32 v[4:5], v[4:5], v[14:15]
	v_med3_f32 v9, v12, s49, v187
	v_med3_f32 v10, v13, s49, v187
	v_med3_f32 v2, v4, s49, v187
	v_med3_f32 v3, v5, s49, v187
	v_cvt_pk_fp8_f32 v6, v9, v10 op_sel:[0,0,1]
	v_cvt_pk_fp8_f32 v7, v2, v3 op_sel:[0,0,1]
	v_lshl_add_u64 v[2:3], v[172:173], 0, s[24:25]
	global_store_dwordx2 v[2:3], v[22:23], off
	v_lshl_add_u64 v[2:3], v[174:175], 0, s[24:25]
	s_andn2_b64 vcc, exec, s[6:7]
	s_mov_b64 s[6:7], -1
	global_store_dwordx2 v[2:3], v[6:7], off
	s_cbranch_vccnz .LBB0_1460
	s_andn2_b64 vcc, exec, s[2:3]
	s_cbranch_vccnz .LBB0_1459
	s_barrier
	s_branch .LBB0_1459

.LBB0_2091:
	s_waitcnt lgkmcnt(0)
	s_load_dwordx4 s[0:3], s[74:75], 0xa8
	v_and_b32_e32 v18, 31, v0
	v_lshlrev_b32_e32 v46, 3, v18
	v_cmp_gt_u32_e64 s[6:7], 24, v18
	s_ashr_i32 s33, s90, 31
	v_lshlrev_b32_e32 v69, 4, v0
	v_cndmask_b32_e64 v2, 0, v46, s[6:7]
	v_lshlrev_b32_e32 v19, 2, v2
	s_waitcnt lgkmcnt(0)
	global_load_dwordx4 v[2:5], v19, s[0:1] offset:784
	global_load_dwordx4 v[6:9], v19, s[2:3] offset:784
	global_load_dwordx4 v[10:13], v19, s[0:1] offset:768
	global_load_dwordx4 v[14:17], v19, s[2:3] offset:768
	s_abs_i32 s0, s90
	v_cvt_f32_u32_e32 v19, s0
	s_sub_i32 s3, 0, s0
	s_add_i32 s1, s90, 0x1ff
	s_ashr_i32 s2, s1, 31
	v_rcp_iflag_f32_e32 v19, v19
	s_abs_i32 s1, s1
	s_xor_b32 s2, s2, s33
	v_mul_f32_e32 v19, 0x4f7ffffe, v19
	v_cvt_u32_f32_e32 v19, v19
	s_barrier
	v_readfirstlane_b32 s4, v19
	s_mul_i32 s3, s3, s4
	s_mul_hi_u32 s3, s4, s3
	s_add_i32 s4, s4, s3
	s_mul_hi_u32 s3, s1, s4
	s_mul_i32 s5, s3, s0
	s_sub_i32 s1, s1, s5
	s_add_i32 s5, s3, 1
	s_sub_i32 s8, s1, s0
	s_cmp_ge_u32 s1, s0
	s_cselect_b32 s3, s5, s3
	s_cselect_b32 s1, s8, s1
	s_add_i32 s5, s3, 1
	s_cmp_ge_u32 s1, s0
	s_cselect_b32 s1, s5, s3
	s_xor_b32 s1, s1, s2
	s_sub_i32 s3, s1, s2
	s_add_i32 s1, s90, 63
	s_ashr_i32 s2, s1, 31
	s_abs_i32 s1, s1
	s_mul_hi_u32 s4, s1, s4
	s_mul_i32 s5, s4, s0
	s_sub_i32 s1, s1, s5
	s_xor_b32 s2, s2, s33
	s_add_i32 s5, s4, 1
	s_sub_i32 s8, s1, s0
	s_cmp_ge_u32 s1, s0
	s_cselect_b32 s4, s5, s4
	s_cselect_b32 s1, s8, s1
	s_add_i32 s5, s4, 1
	s_cmp_ge_u32 s1, s0
	s_cselect_b32 s0, s5, s4
	s_xor_b32 s0, s0, s2
	s_sub_i32 s30, s0, s2
	s_add_i32 s30, s30, s3
	s_cmp_gt_i32 s30, 0
	s_cbranch_scc1 .LBB0_2093
	s_not_b32 s0, s88
	s_mov_b32 s36, s88
	v_lshrrev_b32_e32 v94, 2, v0
	v_and_b32_e32 v48, 48, v69
	s_cbranch_execz .LBB0_2094
	s_branch .LBB0_2150

.LBB0_2094:
	v_and_b32_e32 v19, 24, v0
	v_mul_u32_u24_e32 v27, 0x140, v1
	v_or_b32_e32 v1, 64, v162
	v_cmp_eq_u32_e64 s[8:9], 16, v19
	v_cmp_ne_u32_e64 s[10:11], 16, v19
	v_and_b32_e32 v19, 2, v0
	v_mov_b32_e32 v47, 0
	v_lshrrev_b32_e32 v1, 4, v1
	v_cmp_eq_u32_e64 s[12:13], 0, v19
	v_lshrrev_b32_e32 v19, 5, v162
	v_add_u32_e32 v22, -16, v18
	v_mul_u32_u24_e32 v28, 0x140, v1
	v_xor_b32_e32 v1, v69, v0
	v_lshlrev_b32_e32 v24, 6, v94
	v_mov_b32_e32 v25, v47
	v_lshlrev_b32_e32 v20, 3, v22
	v_cmp_gt_u32_e64 s[14:15], 4, v22
	v_mul_u32_u24_e32 v22, 0xc0, v19
	v_mul_u32_u24_e32 v26, 0x140, v19
	v_lshrrev_b32_e32 v19, 3, v1
	v_lshlrev_b32_e32 v1, 1, v1
	v_lshl_add_u64 v[24:25], s[86:87], 0, v[24:25]
	v_mov_b32_e32 v49, v47
	v_and_b32_e32 v1, 32, v1
	v_lshl_add_u64 v[24:25], v[24:25], 0, v[48:49]
	s_mov_b64 s[4:5], 0x6c800000
	v_and_or_b32 v1, v19, 4, v1
	v_lshl_add_u64 v[50:51], v[24:25], 0, s[4:5]
	v_lshlrev_b32_e32 v18, 4, v18
	v_mov_b32_e32 v19, v47
	v_lshlrev_b32_e32 v24, 1, v22
	v_mov_b32_e32 v25, v47
	v_lshl_add_u64 v[24:25], v[18:19], 0, v[24:25]
	s_mov_b64 s[4:5], 0x45200300
	v_mov_b32_e32 v21, v47
	v_mov_b32_e32 v23, v47
	v_lshl_add_u64 v[52:53], v[24:25], 0, s[4:5]
	v_mov_b64_e32 v[24:25], 0x34401c00
	v_lshl_add_u64 v[54:55], v[20:21], 1, v[24:25]
	v_lshl_add_u64 v[20:21], v[46:47], 0, v[22:23]
	s_mov_b64 s[4:5], 0x45200180
	v_lshl_add_u64 v[56:57], v[20:21], 0, s[4:5]
	v_lshlrev_b32_e32 v20, 1, v26
	v_mov_b32_e32 v21, v47
	v_lshl_add_u64 v[18:19], v[18:19], 0, v[20:21]
	s_mov_b64 s[4:5], 0x4ac00500
	v_lshl_add_u64 v[60:61], v[18:19], 0, s[4:5]
	v_lshlrev_b32_e32 v18, 4, v189
	v_mov_b32_e32 v19, v47
	v_lshlrev_b32_e32 v22, 1, v28
	v_lshl_add_u64 v[22:23], v[18:19], 0, v[22:23]
	s_mov_b64 s[18:19], 0x4ac00180
	v_lshl_add_u64 v[62:63], v[22:23], 0, s[18:19]
	v_lshlrev_b32_e32 v22, 1, v27
	v_mov_b32_e32 v23, v47
	s_add_u32 s0, s86, 0x298000
	v_lshl_add_u64 v[18:19], v[18:19], 0, v[22:23]
	s_addc_u32 s1, s87, 0
	s_not_b32 s2, s88
	v_lshl_add_u64 v[64:65], v[18:19], 0, s[18:19]
	v_lshl_add_u64 v[18:19], v[46:47], 0, v[20:21]
	s_mov_b32 s36, s88
	s_bfe_u32 s2, s92, 0x30006
	v_lshl_add_u64 v[66:67], v[18:19], 0, s[4:5]
	v_mbcnt_lo_u32_b32 v18, -1, 0
	s_lshl_b32 s35, s2, 3
	s_mulk_i32 s2, 0x1800
	v_mbcnt_hi_u32_b32 v96, -1, v18
	v_mul_u32_u24_e32 v1, 0x300, v1
	s_add_i32 s2, s2, 0
	v_and_b32_e32 v18, 64, v96
	v_and_b32_e32 v95, 16, v69
	s_mov_b32 s31, 0
	v_cmp_gt_u32_e64 s[16:17], 32, v162
	s_lshl_b32 s34, s83, 3
	v_add3_u32 v1, 0, v94, v1
	v_lshl_add_u32 v49, v162, 3, s2
	v_lshlrev_b32_e32 v58, 4, v162
	v_mov_b32_e32 v59, v47
	s_mov_b32 s2, 0x3b000000
	s_mov_b32 s37, 0x800000
	v_mov_b32_e32 v68, 0x358637bd
	s_mov_b32 s38, 0xc3e00000
	s_mov_b64 s[4:5], 0xa00
	s_mov_b64 s[22:23], 0x1e00
	s_mov_b64 s[24:25], 0x1000
	v_add_u32_e32 v97, 64, v18
	v_xor_b32_e32 v98, 1, v96
	v_xor_b32_e32 v99, 2, v96
	v_xor_b32_e32 v100, 4, v96
	v_xor_b32_e32 v101, 8, v96
	v_xor_b32_e32 v102, 16, v96
	v_xor_b32_e32 v103, 32, v96
	v_mov_b32_e32 v104, 0xa00
	v_mov_b32_e32 v105, 0x1e00
	v_mov_b32_e32 v106, 0x43e00000
	s_branch .LBB0_2097
